# grid barrier: the acquire invalidate is issued at arrival (CU quiescent until release), nothing waits on it after the release
# speedup vs baseline: 1.0043x; 1.0043x over previous
.LBB0_218:
	s_barrier
	s_waitcnt vmcnt(0)
	s_barrier
	s_mov_b64 s[0:1], exec
	v_readlane_b32 s2, v252, 4
	v_readlane_b32 s3, v252, 5
	s_and_b64 s[2:3], s[0:1], s[2:3]
	v_writelane_b32 v252, s43, 41
	s_mov_b64 exec, s[2:3]
	s_cbranch_execz .LBB0_272
	s_add_i32 s2, 0, 0x22020
	v_mov_b32_e32 v1, s2
	s_waitcnt vmcnt(0) expcnt(0) lgkmcnt(0)
	buffer_inv sc1
	ds_read_b32 v3, v1
	s_add_i32 s2, 0, 0x22024
	v_mov_b32_e32 v1, s2
	ds_read_b32 v1, v1
	s_waitcnt lgkmcnt(1)
	v_cmp_ne_u32_e32 vcc, 0, v3
	s_cbranch_vccnz .LBB0_234
	v_readlane_b32 s4, v252, 1
	v_readlane_b32 s5, v252, 2
	s_load_dwordx2 s[2:3], s[4:5], 0x4
	s_add_u32 s4, s84, 0x4200
	s_addc_u32 s5, s85, 0
	s_add_u32 s6, s84, 0x4400
	s_addc_u32 s7, s85, 0
	s_add_u32 s8, s84, 0x4500
	s_addc_u32 s9, s85, 0
	s_add_u32 s10, s84, 0x4600
	s_addc_u32 s11, s85, 0
	s_add_u32 s12, s84, 0x4700
	s_addc_u32 s13, s85, 0
	s_add_u32 s14, s84, 0x4800
	s_addc_u32 s15, s85, 0
	s_add_u32 s16, s84, 0x4900
	s_addc_u32 s17, s85, 0
	s_add_u32 s18, s84, 0x4a00
	s_addc_u32 s19, s85, 0
	s_add_u32 s20, s84, 0x4b00
	s_addc_u32 s21, s85, 0
	s_add_u32 s22, s84, 0x4c00
	s_addc_u32 s23, s85, 0
	s_add_u32 s24, s84, 0x4d00
	s_addc_u32 s25, s85, 0
	s_add_u32 s26, s84, 0x4e00
	s_addc_u32 s27, s85, 0
	s_add_u32 s28, s84, 0x4f00
	s_addc_u32 s29, s85, 0
	s_add_u32 s30, s84, 0x5000
	s_addc_u32 s31, s85, 0
	s_add_u32 s34, s84, 0x5100
	s_addc_u32 s35, s85, 0
	s_add_u32 s36, s84, 0x5200
	s_addc_u32 s37, s85, 0
	s_waitcnt lgkmcnt(0)
	s_mul_i32 s2, s2, s43
	s_add_u32 s38, s84, 0x5300
	s_mul_i32 s2, s2, s3
	s_addc_u32 s39, s85, 0
	s_mov_b32 s3, 1
	v_mov_b32_e32 v17, 0
	s_branch .LBB0_222

.LBB0_251:
	s_or_b64 exec, exec, s[8:9]
	s_waitcnt vmcnt(0)
	s_waitcnt vmcnt(0)

.LBB0_269:
	s_or_b64 exec, exec, s[6:7]
	s_mov_b64 s[6:7], exec
	v_mbcnt_lo_u32_b32 v1, s6, 0
	v_mbcnt_hi_u32_b32 v1, s7, v1
	v_cmp_eq_u32_e32 vcc, 0, v1
	s_and_saveexec_b64 s[8:9], vcc
	s_cbranch_execz .LBB0_271
	s_bcnt1_i32_b64 s2, s[6:7]
	v_mov_b32_e32 v1, 0x2000
	v_mov_b32_e32 v2, s2

.LBB0_688:
	s_waitcnt vmcnt(63) expcnt(7) lgkmcnt(15)
	s_waitcnt vmcnt(0)
	s_waitcnt vmcnt(0)
	s_barrier
	s_mov_b64 s[0:1], exec
	v_readlane_b32 s2, v252, 4
	v_readlane_b32 s3, v252, 5
	s_and_b64 s[2:3], s[0:1], s[2:3]
	s_mov_b64 exec, s[2:3]
	s_cbranch_execz .LBB0_740
	s_add_i32 s2, 0, 0x22020
	v_mov_b32_e32 v1, s2
	s_waitcnt vmcnt(0) expcnt(0) lgkmcnt(0)
	buffer_inv sc1
	ds_read_b32 v3, v1
	s_add_i32 s2, 0, 0x22024
	v_mov_b32_e32 v1, s2
	ds_read_b32 v1, v1
	s_waitcnt lgkmcnt(1)
	v_cmp_ne_u32_e32 vcc, 0, v3
	s_cbranch_vccnz .LBB0_704
	v_readlane_b32 s4, v252, 1
	v_readlane_b32 s5, v252, 2
	s_load_dwordx2 s[2:3], s[4:5], 0x4
	s_add_u32 s4, s84, 0x4200
	s_addc_u32 s5, s85, 0
	s_add_u32 s6, s84, 0x4400
	s_addc_u32 s7, s85, 0
	s_add_u32 s8, s84, 0x4500
	s_addc_u32 s9, s85, 0
	s_add_u32 s10, s84, 0x4600
	s_addc_u32 s11, s85, 0
	s_add_u32 s12, s84, 0x4700
	s_addc_u32 s13, s85, 0
	s_add_u32 s14, s84, 0x4800
	s_addc_u32 s15, s85, 0
	s_add_u32 s16, s84, 0x4900
	s_addc_u32 s17, s85, 0
	s_add_u32 s18, s84, 0x4a00
	s_addc_u32 s19, s85, 0
	s_add_u32 s20, s84, 0x4b00
	s_addc_u32 s21, s85, 0
	s_add_u32 s22, s84, 0x4c00
	s_addc_u32 s23, s85, 0
	s_add_u32 s24, s84, 0x4d00
	s_addc_u32 s25, s85, 0
	s_add_u32 s26, s84, 0x4e00
	s_addc_u32 s27, s85, 0
	s_add_u32 s28, s84, 0x4f00
	s_addc_u32 s29, s85, 0
	s_add_u32 s30, s84, 0x5000
	s_addc_u32 s31, s85, 0
	s_add_u32 s34, s84, 0x5100
	s_addc_u32 s35, s85, 0
	s_add_u32 s36, s84, 0x5200
	s_addc_u32 s37, s85, 0
	s_waitcnt lgkmcnt(0)
	s_mul_i32 s2, s2, s43
	s_add_u32 s38, s84, 0x5300
	s_mul_i32 s2, s2, s3
	s_addc_u32 s39, s85, 0
	s_mov_b32 s3, 1
	v_mov_b32_e32 v17, 0
	s_branch .LBB0_692

.LBB0_766:
	s_waitcnt vmcnt(0)
	s_waitcnt vmcnt(0)
	s_barrier
	s_mov_b64 s[0:1], exec
	v_readlane_b32 s6, v252, 4
	v_readlane_b32 s7, v252, 5
	s_and_b64 s[6:7], s[0:1], s[6:7]
	s_mov_b64 exec, s[6:7]
	s_cbranch_execz .LBB0_818
	s_add_i32 s6, 0, 0x22020
	v_mov_b32_e32 v1, s6
	s_waitcnt vmcnt(0) expcnt(0) lgkmcnt(0)
	buffer_inv sc1
	ds_read_b32 v3, v1
	s_add_i32 s6, 0, 0x22024
	v_mov_b32_e32 v1, s6
	ds_read_b32 v1, v1
	s_waitcnt lgkmcnt(1)
	v_cmp_ne_u32_e32 vcc, 0, v3
	s_cbranch_vccnz .LBB0_782
	v_readlane_b32 s6, v252, 1
	v_readlane_b32 s7, v252, 2
	s_load_dwordx2 s[10:11], s[6:7], 0x4
	s_add_u32 s6, s84, 0x4200
	s_addc_u32 s7, s85, 0
	s_add_u32 s8, s84, 0x4400
	s_addc_u32 s9, s85, 0
	s_waitcnt lgkmcnt(0)
	s_mul_i32 s33, s10, s43
	s_add_u32 s10, s84, 0x4500
	s_mul_i32 s33, s33, s11
	s_addc_u32 s11, s85, 0
	s_add_u32 s12, s84, 0x4600
	s_addc_u32 s13, s85, 0
	s_add_u32 s14, s84, 0x4700
	s_addc_u32 s15, s85, 0
	s_add_u32 s16, s84, 0x4800
	s_addc_u32 s17, s85, 0
	s_add_u32 s18, s84, 0x4900
	s_addc_u32 s19, s85, 0
	s_add_u32 s20, s84, 0x4a00
	s_addc_u32 s21, s85, 0
	s_add_u32 s22, s84, 0x4b00
	s_addc_u32 s23, s85, 0
	s_add_u32 s24, s84, 0x4c00
	s_addc_u32 s25, s85, 0
	s_add_u32 s26, s84, 0x4d00
	s_addc_u32 s27, s85, 0
	s_add_u32 s28, s84, 0x4e00
	s_addc_u32 s29, s85, 0
	s_add_u32 s30, s84, 0x4f00
	s_addc_u32 s31, s85, 0
	s_add_u32 s34, s84, 0x5000
	s_addc_u32 s35, s85, 0
	s_add_u32 s36, s84, 0x5100
	s_addc_u32 s37, s85, 0
	s_add_u32 s38, s84, 0x5200
	s_addc_u32 s39, s85, 0
	s_add_u32 s40, s84, 0x5300
	s_addc_u32 s41, s85, 0
	s_mov_b32 s52, 1
	v_mov_b32_e32 v17, 0
	s_branch .LBB0_770

.LBB0_797:
	s_or_b64 exec, exec, s[10:11]
	s_waitcnt vmcnt(0)
	s_waitcnt vmcnt(0)

.LBB0_815:
	s_or_b64 exec, exec, s[8:9]
	s_mov_b64 s[8:9], exec
	v_mbcnt_lo_u32_b32 v1, s8, 0
	v_mbcnt_hi_u32_b32 v1, s9, v1
	v_cmp_eq_u32_e32 vcc, 0, v1
	s_and_saveexec_b64 s[10:11], vcc
	s_cbranch_execz .LBB0_817
	s_bcnt1_i32_b64 s8, s[8:9]
	v_mov_b32_e32 v1, 0x2000
	v_mov_b32_e32 v2, s8

.LBB0_839:
	s_waitcnt vmcnt(0)
	s_waitcnt lgkmcnt(0)
	s_barrier
	s_mov_b64 s[0:1], exec
	v_readlane_b32 s6, v252, 4
	v_readlane_b32 s7, v252, 5
	s_and_b64 s[6:7], s[0:1], s[6:7]
	s_mov_b64 exec, s[6:7]
	s_cbranch_execz .LBB0_891
	s_add_i32 s6, 0, 0x22020
	v_mov_b32_e32 v1, s6
	s_waitcnt vmcnt(0) expcnt(0) lgkmcnt(0)
	buffer_inv sc1
	ds_read_b32 v3, v1
	s_add_i32 s6, 0, 0x22024
	v_mov_b32_e32 v1, s6
	ds_read_b32 v1, v1
	s_waitcnt lgkmcnt(1)
	v_cmp_ne_u32_e32 vcc, 0, v3
	s_cbranch_vccnz .LBB0_855
	v_readlane_b32 s6, v252, 1
	v_readlane_b32 s7, v252, 2
	s_load_dwordx2 s[10:11], s[6:7], 0x4
	s_add_u32 s6, s84, 0x4200
	s_addc_u32 s7, s85, 0
	s_add_u32 s8, s84, 0x4400
	s_addc_u32 s9, s85, 0
	s_waitcnt lgkmcnt(0)
	s_mul_i32 s33, s10, s43
	s_add_u32 s10, s84, 0x4500
	s_mul_i32 s33, s33, s11
	s_addc_u32 s11, s85, 0
	s_add_u32 s12, s84, 0x4600
	s_addc_u32 s13, s85, 0
	s_add_u32 s14, s84, 0x4700
	s_addc_u32 s15, s85, 0
	s_add_u32 s16, s84, 0x4800
	s_addc_u32 s17, s85, 0
	s_add_u32 s18, s84, 0x4900
	s_addc_u32 s19, s85, 0
	s_add_u32 s20, s84, 0x4a00
	s_addc_u32 s21, s85, 0
	s_add_u32 s22, s84, 0x4b00
	s_addc_u32 s23, s85, 0
	s_add_u32 s24, s84, 0x4c00
	s_addc_u32 s25, s85, 0
	s_add_u32 s26, s84, 0x4d00
	s_addc_u32 s27, s85, 0
	s_add_u32 s28, s84, 0x4e00
	s_addc_u32 s29, s85, 0
	s_add_u32 s30, s84, 0x4f00
	s_addc_u32 s31, s85, 0
	s_add_u32 s34, s84, 0x5000
	s_addc_u32 s35, s85, 0
	s_add_u32 s36, s84, 0x5100
	s_addc_u32 s37, s85, 0
	s_add_u32 s38, s84, 0x5200
	s_addc_u32 s39, s85, 0
	s_add_u32 s40, s84, 0x5300
	s_addc_u32 s41, s85, 0
	s_mov_b32 s48, 1
	v_mov_b32_e32 v17, 0
	s_branch .LBB0_843

.LBB0_934:
	s_waitcnt vmcnt(0)
	s_barrier
	s_mov_b64 s[0:1], exec
	v_readlane_b32 s4, v252, 4
	v_readlane_b32 s5, v252, 5
	s_and_b64 s[4:5], s[0:1], s[4:5]
	s_mov_b64 exec, s[4:5]
	s_cbranch_execz .LBB0_986
	s_add_i32 s4, 0, 0x22020
	v_mov_b32_e32 v1, s4
	s_waitcnt vmcnt(0) expcnt(0) lgkmcnt(0)
	buffer_inv sc1
	ds_read_b32 v3, v1
	s_add_i32 s4, 0, 0x22024
	v_mov_b32_e32 v1, s4
	ds_read_b32 v1, v1
	s_waitcnt lgkmcnt(1)
	v_cmp_ne_u32_e32 vcc, 0, v3
	s_cbranch_vccnz .LBB0_950
	v_readlane_b32 s4, v252, 1
	v_readlane_b32 s5, v252, 2
	s_load_dwordx2 s[8:9], s[4:5], 0x4
	s_add_u32 s4, s84, 0x4200
	s_addc_u32 s5, s85, 0
	s_add_u32 s6, s84, 0x4400
	s_addc_u32 s7, s85, 0
	s_waitcnt lgkmcnt(0)
	s_mul_i32 s33, s8, s43
	s_add_u32 s8, s84, 0x4500
	s_mul_i32 s33, s33, s9
	s_addc_u32 s9, s85, 0
	s_add_u32 s10, s84, 0x4600
	s_addc_u32 s11, s85, 0
	s_add_u32 s12, s84, 0x4700
	s_addc_u32 s13, s85, 0
	s_add_u32 s14, s84, 0x4800
	s_addc_u32 s15, s85, 0
	s_add_u32 s16, s84, 0x4900
	s_addc_u32 s17, s85, 0
	s_add_u32 s18, s84, 0x4a00
	s_addc_u32 s19, s85, 0
	s_add_u32 s20, s84, 0x4b00
	s_addc_u32 s21, s85, 0
	s_add_u32 s22, s84, 0x4c00
	s_addc_u32 s23, s85, 0
	s_add_u32 s24, s84, 0x4d00
	s_addc_u32 s25, s85, 0
	s_add_u32 s26, s84, 0x4e00
	s_addc_u32 s27, s85, 0
	s_add_u32 s28, s84, 0x4f00
	s_addc_u32 s29, s85, 0
	s_add_u32 s30, s84, 0x5000
	s_addc_u32 s31, s85, 0
	s_add_u32 s34, s84, 0x5100
	s_addc_u32 s35, s85, 0
	s_add_u32 s36, s84, 0x5200
	s_addc_u32 s37, s85, 0
	s_add_u32 s38, s84, 0x5300
	s_addc_u32 s39, s85, 0
	s_mov_b32 s46, 1
	v_mov_b32_e32 v17, 0
	s_branch .LBB0_938

.LBB0_983:
	s_or_b64 exec, exec, s[6:7]
	s_mov_b64 s[6:7], exec
	v_mbcnt_lo_u32_b32 v1, s6, 0
	v_mbcnt_hi_u32_b32 v1, s7, v1
	v_cmp_eq_u32_e32 vcc, 0, v1
	s_and_saveexec_b64 s[8:9], vcc
	s_cbranch_execz .LBB0_985
	s_bcnt1_i32_b64 s6, s[6:7]
	v_mov_b32_e32 v1, 0x2000
	v_mov_b32_e32 v2, s6

.LBB0_1017:
	s_waitcnt vmcnt(0)
	s_waitcnt vmcnt(0)
	s_barrier
	s_mov_b64 s[0:1], exec
	v_readlane_b32 s4, v252, 4
	v_readlane_b32 s5, v252, 5
	s_and_b64 s[4:5], s[0:1], s[4:5]
	s_mov_b64 exec, s[4:5]
	s_cbranch_execz .LBB0_1069
	s_add_i32 s4, 0, 0x22020
	v_mov_b32_e32 v1, s4
	s_waitcnt vmcnt(0) expcnt(0) lgkmcnt(0)
	buffer_inv sc1
	ds_read_b32 v3, v1
	s_add_i32 s4, 0, 0x22024
	v_mov_b32_e32 v1, s4
	ds_read_b32 v1, v1
	s_waitcnt lgkmcnt(1)
	v_cmp_ne_u32_e32 vcc, 0, v3
	s_cbranch_vccnz .LBB0_1033
	v_readlane_b32 s4, v252, 1
	v_readlane_b32 s5, v252, 2
	s_load_dwordx2 s[8:9], s[4:5], 0x4
	s_add_u32 s4, s84, 0x4200
	s_addc_u32 s5, s85, 0
	s_add_u32 s6, s84, 0x4400
	s_addc_u32 s7, s85, 0
	s_waitcnt lgkmcnt(0)
	s_mul_i32 s33, s8, s43
	s_add_u32 s8, s84, 0x4500
	s_mul_i32 s33, s33, s9
	s_addc_u32 s9, s85, 0
	s_add_u32 s10, s84, 0x4600
	s_addc_u32 s11, s85, 0
	s_add_u32 s12, s84, 0x4700
	s_addc_u32 s13, s85, 0
	s_add_u32 s14, s84, 0x4800
	s_addc_u32 s15, s85, 0
	s_add_u32 s16, s84, 0x4900
	s_addc_u32 s17, s85, 0
	s_add_u32 s18, s84, 0x4a00
	s_addc_u32 s19, s85, 0
	s_add_u32 s20, s84, 0x4b00
	s_addc_u32 s21, s85, 0
	s_add_u32 s22, s84, 0x4c00
	s_addc_u32 s23, s85, 0
	s_add_u32 s24, s84, 0x4d00
	s_addc_u32 s25, s85, 0
	s_add_u32 s26, s84, 0x4e00
	s_addc_u32 s27, s85, 0
	s_add_u32 s28, s84, 0x4f00
	s_addc_u32 s29, s85, 0
	s_add_u32 s30, s84, 0x5000
	s_addc_u32 s31, s85, 0
	s_add_u32 s34, s84, 0x5100
	s_addc_u32 s35, s85, 0
	s_add_u32 s36, s84, 0x5200
	s_addc_u32 s37, s85, 0
	s_add_u32 s38, s84, 0x5300
	s_addc_u32 s39, s85, 0
	s_mov_b32 s46, 1
	v_mov_b32_e32 v17, 0
	s_branch .LBB0_1021

.LBB0_1112:
	s_waitcnt vmcnt(0)
	s_waitcnt lgkmcnt(0)
	s_barrier
	s_mov_b64 s[4:5], exec
	v_readlane_b32 s8, v252, 4
	v_readlane_b32 s9, v252, 5
	s_and_b64 s[8:9], s[4:5], s[8:9]
	s_mov_b64 exec, s[8:9]
	s_cbranch_execz .LBB0_1164
	s_add_i32 s8, 0, 0x22020
	v_mov_b32_e32 v1, s8
	s_waitcnt vmcnt(0) expcnt(0) lgkmcnt(0)
	buffer_inv sc1
	ds_read_b32 v3, v1
	s_add_i32 s8, 0, 0x22024
	v_mov_b32_e32 v1, s8
	ds_read_b32 v1, v1
	s_waitcnt lgkmcnt(1)
	v_cmp_ne_u32_e32 vcc, 0, v3
	s_cbranch_vccnz .LBB0_1128
	v_readlane_b32 s8, v252, 1
	v_readlane_b32 s9, v252, 2
	s_load_dwordx2 s[12:13], s[8:9], 0x4
	s_add_u32 s8, s84, 0x4200
	s_addc_u32 s9, s85, 0
	s_add_u32 s10, s84, 0x4400
	s_addc_u32 s11, s85, 0
	s_waitcnt lgkmcnt(0)
	s_mul_i32 s33, s12, s43
	s_add_u32 s12, s84, 0x4500
	s_mul_i32 s33, s33, s13
	s_addc_u32 s13, s85, 0
	s_add_u32 s14, s84, 0x4600
	s_addc_u32 s15, s85, 0
	s_add_u32 s16, s84, 0x4700
	s_addc_u32 s17, s85, 0
	s_add_u32 s18, s84, 0x4800
	s_addc_u32 s19, s85, 0
	s_add_u32 s20, s84, 0x4900
	s_addc_u32 s21, s85, 0
	s_add_u32 s22, s84, 0x4a00
	s_addc_u32 s23, s85, 0
	s_add_u32 s24, s84, 0x4b00
	s_addc_u32 s25, s85, 0
	s_add_u32 s26, s84, 0x4c00
	s_addc_u32 s27, s85, 0
	s_add_u32 s28, s84, 0x4d00
	s_addc_u32 s29, s85, 0
	s_add_u32 s30, s84, 0x4e00
	s_addc_u32 s31, s85, 0
	s_add_u32 s34, s84, 0x4f00
	s_addc_u32 s35, s85, 0
	s_add_u32 s36, s84, 0x5000
	s_addc_u32 s37, s85, 0
	s_add_u32 s38, s84, 0x5100
	s_addc_u32 s39, s85, 0
	s_add_u32 s40, s84, 0x5200
	s_addc_u32 s41, s85, 0
	s_add_u32 s42, s84, 0x5300
	s_addc_u32 s43, s85, 0
	s_mov_b32 s50, 1
	v_mov_b32_e32 v17, 0
	s_branch .LBB0_1116

.LBB0_1143:
	s_or_b64 exec, exec, s[12:13]
	s_waitcnt vmcnt(0)
	s_waitcnt vmcnt(0)

.LBB0_1161:
	s_or_b64 exec, exec, s[10:11]
	s_mov_b64 s[10:11], exec
	v_mbcnt_lo_u32_b32 v1, s10, 0
	v_mbcnt_hi_u32_b32 v1, s11, v1
	v_cmp_eq_u32_e32 vcc, 0, v1
	s_and_saveexec_b64 s[12:13], vcc
	s_cbranch_execz .LBB0_1163
	s_bcnt1_i32_b64 s10, s[10:11]
	v_mov_b32_e32 v1, 0x2000
	v_mov_b32_e32 v2, s10

.LBB0_1266:
	s_waitcnt vmcnt(0)
	s_barrier
	s_mov_b64 s[0:1], exec
	v_readlane_b32 s4, v252, 4
	v_readlane_b32 s5, v252, 5
	s_and_b64 s[4:5], s[0:1], s[4:5]
	s_mov_b64 exec, s[4:5]
	s_cbranch_execz .LBB0_1318
	s_add_i32 s4, 0, 0x22020
	v_mov_b32_e32 v1, s4
	s_waitcnt vmcnt(0) expcnt(0) lgkmcnt(0)
	buffer_inv sc1
	ds_read_b32 v3, v1
	s_add_i32 s4, 0, 0x22024
	v_mov_b32_e32 v1, s4
	ds_read_b32 v1, v1
	s_waitcnt lgkmcnt(1)
	v_cmp_ne_u32_e32 vcc, 0, v3
	s_cbranch_vccnz .LBB0_1282
	v_readlane_b32 s4, v252, 1
	v_readlane_b32 s5, v252, 2
	s_load_dwordx2 s[8:9], s[4:5], 0x4
	s_add_u32 s4, s84, 0x4200
	s_addc_u32 s5, s85, 0
	s_add_u32 s6, s84, 0x4400
	s_addc_u32 s7, s85, 0
	s_waitcnt lgkmcnt(0)
	s_mul_i32 s33, s8, s43
	s_add_u32 s8, s84, 0x4500
	s_mul_i32 s33, s33, s9
	s_addc_u32 s9, s85, 0
	s_add_u32 s10, s84, 0x4600
	s_addc_u32 s11, s85, 0
	s_add_u32 s12, s84, 0x4700
	s_addc_u32 s13, s85, 0
	s_add_u32 s14, s84, 0x4800
	s_addc_u32 s15, s85, 0
	s_add_u32 s16, s84, 0x4900
	s_addc_u32 s17, s85, 0
	s_add_u32 s20, s84, 0x4a00
	s_addc_u32 s21, s85, 0
	s_add_u32 s22, s84, 0x4b00
	s_addc_u32 s23, s85, 0
	s_add_u32 s24, s84, 0x4c00
	s_addc_u32 s25, s85, 0
	s_add_u32 s26, s84, 0x4d00
	s_addc_u32 s27, s85, 0
	s_add_u32 s28, s84, 0x4e00
	s_addc_u32 s29, s85, 0
	s_add_u32 s30, s84, 0x4f00
	s_addc_u32 s31, s85, 0
	s_add_u32 s34, s84, 0x5000
	s_addc_u32 s35, s85, 0
	s_add_u32 s36, s84, 0x5100
	s_addc_u32 s37, s85, 0
	s_add_u32 s38, s84, 0x5200
	s_addc_u32 s39, s85, 0
	s_add_u32 s40, s84, 0x5300
	s_addc_u32 s41, s85, 0
	s_mov_b32 s48, 1
	v_mov_b32_e32 v17, 0
	s_branch .LBB0_1270

.LBB0_1356:
	s_waitcnt vmcnt(0)
	s_waitcnt vmcnt(0)
	s_barrier
	s_mov_b64 s[4:5], exec
	v_readlane_b32 s6, v252, 4
	v_readlane_b32 s7, v252, 5
	s_and_b64 s[6:7], s[4:5], s[6:7]
	s_mov_b64 exec, s[6:7]
	s_cbranch_execz .LBB0_1408
	s_add_i32 s6, 0, 0x22020
	v_mov_b32_e32 v1, s6
	s_waitcnt vmcnt(0) expcnt(0) lgkmcnt(0)
	buffer_inv sc1
	ds_read_b32 v3, v1
	s_add_i32 s6, 0, 0x22024
	v_mov_b32_e32 v1, s6
	ds_read_b32 v1, v1
	s_waitcnt lgkmcnt(1)
	v_cmp_ne_u32_e32 vcc, 0, v3
	s_cbranch_vccnz .LBB0_1372
	v_readlane_b32 s6, v252, 1
	v_readlane_b32 s7, v252, 2
	s_load_dwordx2 s[10:11], s[6:7], 0x4
	s_add_u32 s6, s84, 0x4200
	s_addc_u32 s7, s85, 0
	s_add_u32 s8, s84, 0x4400
	s_addc_u32 s9, s85, 0
	s_waitcnt lgkmcnt(0)
	s_mul_i32 s33, s10, s43
	s_add_u32 s10, s84, 0x4500
	s_mul_i32 s33, s33, s11
	s_addc_u32 s11, s85, 0
	s_add_u32 s12, s84, 0x4600
	s_addc_u32 s13, s85, 0
	s_add_u32 s14, s84, 0x4700
	s_addc_u32 s15, s85, 0
	s_add_u32 s16, s84, 0x4800
	s_addc_u32 s17, s85, 0
	s_add_u32 s18, s84, 0x4900
	s_addc_u32 s19, s85, 0
	s_add_u32 s20, s84, 0x4a00
	s_addc_u32 s21, s85, 0
	s_add_u32 s22, s84, 0x4b00
	s_addc_u32 s23, s85, 0
	s_add_u32 s24, s84, 0x4c00
	s_addc_u32 s25, s85, 0
	s_add_u32 s26, s84, 0x4d00
	s_addc_u32 s27, s85, 0
	s_add_u32 s28, s84, 0x4e00
	s_addc_u32 s29, s85, 0
	s_add_u32 s30, s84, 0x4f00
	s_addc_u32 s31, s85, 0
	s_add_u32 s34, s84, 0x5000
	s_addc_u32 s35, s85, 0
	s_add_u32 s36, s84, 0x5100
	s_addc_u32 s37, s85, 0
	s_add_u32 s38, s84, 0x5200
	s_addc_u32 s39, s85, 0
	s_add_u32 s40, s84, 0x5300
	s_addc_u32 s41, s85, 0
	s_mov_b32 s48, 1
	v_mov_b32_e32 v17, 0
	s_branch .LBB0_1360

.LBB0_1426:
	s_waitcnt vmcnt(0)
	s_waitcnt vmcnt(0)
	s_barrier
	s_mov_b64 s[0:1], exec
	v_readlane_b32 s2, v252, 4
	v_readlane_b32 s3, v252, 5
	s_and_b64 s[2:3], s[0:1], s[2:3]
	s_mov_b64 exec, s[2:3]
	s_cbranch_execz .LBB0_1478
	s_add_i32 s2, 0, 0x22020
	v_mov_b32_e32 v1, s2
	s_waitcnt vmcnt(0) expcnt(0) lgkmcnt(0)
	buffer_inv sc1
	ds_read_b32 v3, v1
	s_add_i32 s2, 0, 0x22024
	v_mov_b32_e32 v1, s2
	ds_read_b32 v1, v1
	s_waitcnt lgkmcnt(1)
	v_cmp_ne_u32_e32 vcc, 0, v3
	s_cbranch_vccnz .LBB0_1442
	v_readlane_b32 s2, v252, 1
	v_readlane_b32 s3, v252, 2
	s_load_dwordx2 s[8:9], s[2:3], 0x4
	s_add_u32 s2, s84, 0x4200
	s_addc_u32 s3, s85, 0
	s_add_u32 s6, s84, 0x4400
	s_addc_u32 s7, s85, 0
	s_waitcnt lgkmcnt(0)
	s_mul_i32 s33, s8, s43
	s_add_u32 s8, s84, 0x4500
	s_mul_i32 s33, s33, s9
	s_addc_u32 s9, s85, 0
	s_add_u32 s10, s84, 0x4600
	s_addc_u32 s11, s85, 0
	s_add_u32 s12, s84, 0x4700
	s_addc_u32 s13, s85, 0
	s_add_u32 s14, s84, 0x4800
	s_addc_u32 s15, s85, 0
	s_add_u32 s16, s84, 0x4900
	s_addc_u32 s17, s85, 0
	s_add_u32 s18, s84, 0x4a00
	s_addc_u32 s19, s85, 0
	s_add_u32 s20, s84, 0x4b00
	s_addc_u32 s21, s85, 0
	s_add_u32 s22, s84, 0x4c00
	s_addc_u32 s23, s85, 0
	s_add_u32 s24, s84, 0x4d00
	s_addc_u32 s25, s85, 0
	s_add_u32 s26, s84, 0x4e00
	s_addc_u32 s27, s85, 0
	s_add_u32 s28, s84, 0x4f00
	s_addc_u32 s29, s85, 0
	s_add_u32 s30, s84, 0x5000
	s_addc_u32 s31, s85, 0
	s_add_u32 s34, s84, 0x5100
	s_addc_u32 s35, s85, 0
	s_add_u32 s36, s84, 0x5200
	s_addc_u32 s37, s85, 0
	s_add_u32 s38, s84, 0x5300
	s_addc_u32 s39, s85, 0
	s_mov_b32 s46, 1
	v_mov_b32_e32 v17, 0
	s_branch .LBB0_1430
